# v85 + P11 items remapped so that the 8 waves of a workgroup rank the same head at the same time (their 64 KB sub-key operand loads hit the CU's L1 instead of 8 separate L2 streams)
# speedup vs baseline: 1.0077x; 1.0077x over previous
; #define LAS __attribute__((address_space(3)))
; __device__ __forceinline__ void p11_route(Frame& F) {
;     const bf16* QRY = (const bf16*)(F.ws + WS_QRY); const bf16* SK = (const bf16*)(F.ws + WS_SUBK);
;     int* PIDX = (int*)(F.ws + WS_PIDX); float* PGT = (float*)(F.ws + WS_PG);
;     LAS float* sc = (LAS float*)(F.lds + F.wave * 16640);
;     LAS int* ptab = (LAS int*)(F.lds + 8 * 16640);
;     if (F.tid < 50) { const int l = F.tid; const int ci = l < 16 ? 0 : l < 24 ? 1 : l < 29 ? 2 : l < 33 ? 3 : l < 36 ? 4 : l < 38 ? 5 : l < 40 ? 6 : l < 42 ? 7 : l - 34;
;         const int cj = l < 16 ? l : l < 24 ? l - 16 : l < 29 ? l - 24 : l < 33 ? l - 29 : l < 36 ? l - 33 : l < 38 ? l - 36 : l < 40 ? l - 38 : l < 42 ? l - 40 : 0; ptab[l] = ci * 16 + cj; }
;     __syncthreads();
;     const int g = F.lane >> 4, l15 = F.lane & 15;
;     for (int item = F.gw; item < (S_ / 16) * PH; item += F.NGW) {
;         const int tile = item >> 3, h = item & 7, t0 = tile * 16;
; #pragma unroll
;         for (int c = 0; c < 2; ++c) {
;             f32x4 acc[8];
; #pragma unroll
;             for (int nt = 0; nt < 8; ++nt) acc[nt] = (f32x4){0.f, 0.f, 0.f, 0.f};
; #pragma unroll
;             for (int ks = 0; ks < 4; ++ks) { const gbf16x8 a = *(const gbf16x8*)(QRY + (size_t)(t0 + l15) * 2048 + h * 256 + c * 128 + 32 * ks + 8 * g);
; #pragma unroll
;                 for (int nt = 0; nt < 8; ++nt) acc[nt] = __builtin_amdgcn_mfma_f32_16x16x32_bf16(a, *(const gbf16x8*)(SK + ((size_t)(h * 2 + c) * PNK + 16 * nt + l15) * 128 + 32 * ks + 8 * g), acc[nt], 0, 0, 0); }
.LBB0_3211:
	s_or_b64 exec, exec, s[10:11]
	s_cmpk_gt_i32 s94, 0xfff
	s_waitcnt lgkmcnt(0)
	s_barrier
	s_cbranch_scc1 .LBB0_3220
	s_waitcnt vmcnt(10)
	v_ashrrev_i32_e32 v6, 4, v1
	v_lshlrev_b32_e32 v2, 3, v6
	v_ashrrev_i32_e32 v3, 31, v2
	v_lshlrev_b64 v[2:3], 1, v[2:3]
	v_lshl_add_u64 v[4:5], s[68:69], 0, v[2:3]
	s_mov_b64 s[0:1], 0x200000
	v_lshl_add_u64 v[76:77], v[4:5], 0, s[0:1]
	s_mov_b64 s[0:1], 0x200040
	v_lshl_add_u64 v[92:93], v[4:5], 0, s[0:1]
	s_mov_b64 s[0:1], 0x200080
	v_lshl_add_u64 v[108:109], v[4:5], 0, s[0:1]
	s_mov_b64 s[0:1], 0x2000c0
	s_mul_i32 s12, s66, 0x4100
	v_and_b32_e32 v150, 15, v1
	v_lshl_add_u64 v[124:125], v[4:5], 0, s[0:1]
	s_movk_i32 s0, 0x810
	s_add_i32 s4, s12, 0
	v_lshlrev_b32_e32 v7, 2, v150
	v_mul_lo_u32 v4, v6, s0
	v_add3_u32 v151, s4, v7, v4
	v_and_b32_e32 v128, 31, v1
	v_lshlrev_b32_e32 v4, 1, v1
	s_movk_i32 s13, 0x204
	v_mov_b32_e32 v5, s4
	s_add_u32 s6, s68, 0x800000
	v_mad_u32_u24 v152, v128, s13, v5
	v_and_b32_e32 v129, 0xffffffc0, v4
	v_lshlrev_b32_e32 v4, 2, v1
	s_movk_i32 s0, 0x80
	v_bfrev_b32_e32 v5, 0.5
	s_addc_u32 s7, s69, 0
	v_bitop3_b32 v153, v4, s0, v5 bitop3:0x6c
	v_mul_lo_u32 v4, v1, s13
	s_bfe_u32 s8, s94, 0x30003
	v_add_u32_e32 v154, s4, v4
	s_lshl_b32 s4, s8, 9
	s_add_u32 s4, s68, s4
	s_addc_u32 s5, s69, 0
	v_lshl_add_u64 v[2:3], s[4:5], 0, v[2:3]
	s_mov_b64 s[4:5], 0x2b400000
	v_lshl_add_u64 v[2:3], v[2:3], 0, s[4:5]
	s_lshl_b32 s4, s8, 6
	v_lshlrev_b32_e32 v4, 8, v150
	s_add_u32 s4, s68, s4
	v_lshl_or_b32 v126, s8, 16, v4
	v_mov_b32_e32 v127, 0
	s_addc_u32 s5, s69, 0
	v_lshl_add_u64 v[4:5], v[76:77], 0, v[126:127]
	s_waitcnt vmcnt(0)
	v_or_b32_e32 v48, 0x1000, v126
	v_mov_b32_e32 v49, v127
	v_or_b32_e32 v50, 0x2000, v126
	v_mov_b32_e32 v51, v127
	v_or_b32_e32 v52, 0x3000, v126
	v_mov_b32_e32 v53, v127
	v_or_b32_e32 v54, 0x4000, v126
	v_mov_b32_e32 v55, v127
	v_or_b32_e32 v56, 0x5000, v126
	v_mov_b32_e32 v57, v127
	v_or_b32_e32 v58, 0x6000, v126
	v_mov_b32_e32 v59, v127
	v_or_b32_e32 v60, 0x7000, v126
	v_mov_b32_e32 v61, v127
	v_or_b32_e32 v110, 0x8000, v126
	v_mov_b32_e32 v111, v127
	v_or_b32_e32 v112, 0x9000, v126
	v_mov_b32_e32 v113, v127
	v_or_b32_e32 v114, 0xa000, v126
	v_mov_b32_e32 v115, v127
	v_or_b32_e32 v116, 0xb000, v126
	v_mov_b32_e32 v117, v127
	v_or_b32_e32 v118, 0xc000, v126
	v_mov_b32_e32 v119, v127
	v_or_b32_e32 v120, 0xd000, v126
	v_mov_b32_e32 v121, v127
	v_or_b32_e32 v122, 0xe000, v126
	v_mov_b32_e32 v123, v127
	v_or_b32_e32 v126, 0xf000, v126
	s_add_u32 s8, s4, 0xe00000
	v_lshl_add_u64 v[6:7], v[76:77], 0, v[48:49]
	v_lshl_add_u64 v[8:9], v[76:77], 0, v[50:51]
	v_lshl_add_u64 v[10:11], v[76:77], 0, v[52:53]
	v_lshl_add_u64 v[12:13], v[76:77], 0, v[54:55]
	v_lshl_add_u64 v[14:15], v[76:77], 0, v[56:57]
	v_lshl_add_u64 v[16:17], v[76:77], 0, v[58:59]
	v_lshl_add_u64 v[18:19], v[76:77], 0, v[60:61]
	v_lshl_add_u64 v[20:21], v[92:93], 0, v[48:49]
	v_lshl_add_u64 v[22:23], v[92:93], 0, v[50:51]
	v_lshl_add_u64 v[24:25], v[92:93], 0, v[52:53]
	v_lshl_add_u64 v[26:27], v[92:93], 0, v[54:55]
	v_lshl_add_u64 v[28:29], v[92:93], 0, v[56:57]
	v_lshl_add_u64 v[30:31], v[92:93], 0, v[58:59]
	v_lshl_add_u64 v[32:33], v[92:93], 0, v[60:61]
	v_lshl_add_u64 v[34:35], v[108:109], 0, v[48:49]
	v_lshl_add_u64 v[36:37], v[108:109], 0, v[50:51]
	v_lshl_add_u64 v[38:39], v[108:109], 0, v[52:53]
	v_lshl_add_u64 v[40:41], v[108:109], 0, v[54:55]
	v_lshl_add_u64 v[42:43], v[108:109], 0, v[56:57]
	v_lshl_add_u64 v[44:45], v[108:109], 0, v[58:59]
	v_lshl_add_u64 v[46:47], v[108:109], 0, v[60:61]
	v_lshl_add_u64 v[48:49], v[124:125], 0, v[48:49]
	v_lshl_add_u64 v[50:51], v[124:125], 0, v[50:51]
	v_lshl_add_u64 v[52:53], v[124:125], 0, v[52:53]
	v_lshl_add_u64 v[54:55], v[124:125], 0, v[54:55]
	v_lshl_add_u64 v[56:57], v[124:125], 0, v[56:57]
	v_lshl_add_u64 v[58:59], v[124:125], 0, v[58:59]
	v_lshl_add_u64 v[60:61], v[124:125], 0, v[60:61]
	v_lshl_add_u64 v[62:63], v[76:77], 0, v[110:111]
	v_lshl_add_u64 v[64:65], v[76:77], 0, v[112:113]
	v_lshl_add_u64 v[66:67], v[76:77], 0, v[114:115]
	v_lshl_add_u64 v[68:69], v[76:77], 0, v[116:117]
	v_lshl_add_u64 v[70:71], v[76:77], 0, v[118:119]
	v_lshl_add_u64 v[72:73], v[76:77], 0, v[120:121]
	v_lshl_add_u64 v[74:75], v[76:77], 0, v[122:123]
	v_lshl_add_u64 v[76:77], v[76:77], 0, v[126:127]
	v_lshl_add_u64 v[78:79], v[92:93], 0, v[110:111]
	v_lshl_add_u64 v[80:81], v[92:93], 0, v[112:113]
	v_lshl_add_u64 v[82:83], v[92:93], 0, v[114:115]
	v_lshl_add_u64 v[84:85], v[92:93], 0, v[116:117]
	v_lshl_add_u64 v[86:87], v[92:93], 0, v[118:119]
	v_lshl_add_u64 v[88:89], v[92:93], 0, v[120:121]
	v_lshl_add_u64 v[90:91], v[92:93], 0, v[122:123]
	v_lshl_add_u64 v[92:93], v[92:93], 0, v[126:127]
	v_lshl_add_u64 v[94:95], v[108:109], 0, v[110:111]
	v_lshl_add_u64 v[96:97], v[108:109], 0, v[112:113]
	v_lshl_add_u64 v[98:99], v[108:109], 0, v[114:115]
	v_lshl_add_u64 v[100:101], v[108:109], 0, v[116:117]
	v_lshl_add_u64 v[102:103], v[108:109], 0, v[118:119]
	v_lshl_add_u64 v[104:105], v[108:109], 0, v[120:121]
	v_lshl_add_u64 v[106:107], v[108:109], 0, v[122:123]
	v_lshl_add_u64 v[108:109], v[108:109], 0, v[126:127]
	v_lshl_add_u64 v[110:111], v[124:125], 0, v[110:111]
	v_lshl_add_u64 v[112:113], v[124:125], 0, v[112:113]
	v_lshl_add_u64 v[114:115], v[124:125], 0, v[114:115]
	v_lshl_add_u64 v[116:117], v[124:125], 0, v[116:117]
	v_lshl_add_u64 v[118:119], v[124:125], 0, v[118:119]
	v_lshl_add_u64 v[120:121], v[124:125], 0, v[120:121]
	v_lshl_add_u64 v[122:123], v[124:125], 0, v[122:123]
	v_lshl_add_u64 v[124:125], v[124:125], 0, v[126:127]
	s_addc_u32 s9, s5, 0
	v_mov_b32_e32 v126, s12
	v_lshlrev_b32_e32 v127, 3, v1
	s_add_u32 s10, s4, 0x1200000
	v_mad_u32_u24 v126, v128, s13, v126
	v_and_b32_e32 v127, 0xffffff00, v127
	v_cmp_gt_i32_e64 s[0:1], 32, v1
	v_cmp_gt_i32_e64 s[2:3], 16, v1
	s_addc_u32 s11, s5, 0
	s_movk_i32 s14, 0xff00
	v_add3_u32 v155, v126, v127, 0
	v_sub_u32_e32 v156, 0xfc, v129
	v_mov_b32_e32 v157, 0x358637bd
	s_mov_b32 s15, 0xf800000
	v_mov_b32_e32 v158, 0x260
	s_add_i32 s16, 0, 0x20800
	s_mov_b32 s17, s94
	s_branch .LBB0_3214

; __device__ __forceinline__ void p11_route(Frame& F) {
;     ...
;     for (int item = F.gw; item < (S_ / 16) * PH; item += F.NGW) {
;         const int tile = item >> 3, h = item & 7, t0 = tile * 16;
; #pragma unroll
;         for (int c = 0; c < 2; ++c) {
;             f32x4 acc[8];
; #pragma unroll
;             for (int nt = 0; nt < 8; ++nt) acc[nt] = (f32x4){0.f, 0.f, 0.f, 0.f};
; #pragma unroll
;             for (int ks = 0; ks < 4; ++ks) { const gbf16x8 a = *(const gbf16x8*)(QRY + (size_t)(t0 + l15) * 2048 + h * 256 + c * 128 + 32 * ks + 8 * g);
; #pragma unroll
;                 for (int nt = 0; nt < 8; ++nt) acc[nt] = __builtin_amdgcn_mfma_f32_16x16x32_bf16(a, *(const gbf16x8*)(SK + ((size_t)(h * 2 + c) * PNK + 16 * nt + l15) * 128 + 32 * ks + 8 * g), acc[nt], 0, 0, 0); }
; #pragma unroll
;             for (int nt = 0; nt < 8; ++nt)
; #pragma unroll
;                 for (int r = 0; r < 4; ++r) sc[(c * 16 + 4 * g + r) * 129 + 16 * nt + l15] = acc[nt][r];
.LBB0_3214:
	s_and_b32 s4, s17, 0x7ff
	s_lshr_b32 s18, s4, 6
	s_lshl_b32 s18, s18, 4
	s_and_b32 s4, s4, 7
	s_lshl_b32 s4, s4, 1
	s_add_i32 s18, s18, s4
	s_lshr_b32 s4, s17, 11
	s_add_i32 s18, s18, s4
	s_lshl_b32 s18, s18, 4
	s_waitcnt lgkmcnt(0)
	v_or_b32_e32 v126, s18, v150
	v_ashrrev_i32_e32 v127, 31, v126
	v_lshlrev_b64 v[126:127], 12, v[126:127]
	v_lshl_add_u64 v[126:127], v[2:3], 0, v[126:127]
	global_load_dwordx4 v[128:131], v[126:127], off
	global_load_dwordx4 v[132:135], v[4:5], off
	global_load_dwordx4 v[136:139], v[6:7], off
	global_load_dwordx4 v[140:143], v[8:9], off
	global_load_dwordx4 v[144:147], v[10:11], off
	global_load_dwordx4 v[160:163], v[12:13], off
	global_load_dwordx4 v[164:167], v[14:15], off
	global_load_dwordx4 v[168:171], v[16:17], off
	global_load_dwordx4 v[172:175], v[18:19], off
	global_load_dwordx4 v[176:179], v[126:127], off offset:64
	global_load_dwordx4 v[180:183], v[4:5], off offset:64
	global_load_dwordx4 v[184:187], v[20:21], off
	global_load_dwordx4 v[188:191], v[22:23], off
	global_load_dwordx4 v[192:195], v[24:25], off
	global_load_dwordx4 v[196:199], v[26:27], off
	global_load_dwordx4 v[200:203], v[28:29], off
	global_load_dwordx4 v[204:207], v[30:31], off
	global_load_dwordx4 v[208:211], v[32:33], off
	global_load_dwordx4 v[212:215], v[126:127], off offset:128
	global_load_dwordx4 v[216:219], v[4:5], off offset:128
	global_load_dwordx4 v[220:223], v[34:35], off
	global_load_dwordx4 v[224:227], v[36:37], off
	global_load_dwordx4 v[228:231], v[38:39], off
	global_load_dwordx4 v[232:235], v[40:41], off
	global_load_dwordx4 v[236:239], v[42:43], off
	global_load_dwordx4 v[240:243], v[44:45], off
	global_load_dwordx4 v[244:247], v[46:47], off
	s_mov_b32 s4, 0
	v_mov_b32_e32 v148, 0xff800000
	v_mov_b32_e32 v149, 0xff800000
	v_mov_b32_e32 v159, 0xff800000
	s_waitcnt vmcnt(25)
	v_mfma_f32_16x16x32_bf16 v[132:135], v[128:131], v[132:135], 0
	s_waitcnt vmcnt(24)
	v_mfma_f32_16x16x32_bf16 v[136:139], v[128:131], v[136:139], 0
	s_waitcnt vmcnt(23)
	v_mfma_f32_16x16x32_bf16 v[140:143], v[128:131], v[140:143], 0
	s_waitcnt vmcnt(22)
	v_mfma_f32_16x16x32_bf16 v[144:147], v[128:131], v[144:147], 0
	s_waitcnt vmcnt(21)
	v_mfma_f32_16x16x32_bf16 v[160:163], v[128:131], v[160:163], 0
	s_waitcnt vmcnt(20)
	v_mfma_f32_16x16x32_bf16 v[164:167], v[128:131], v[164:167], 0
	s_waitcnt vmcnt(19)
	v_mfma_f32_16x16x32_bf16 v[168:171], v[128:131], v[168:171], 0
	s_waitcnt vmcnt(18)
	v_mfma_f32_16x16x32_bf16 v[128:131], v[128:131], v[172:175], 0
	s_waitcnt vmcnt(16)
	v_mfma_f32_16x16x32_bf16 v[132:135], v[176:179], v[180:183], v[132:135]
	s_waitcnt vmcnt(15)
	v_mfma_f32_16x16x32_bf16 v[136:139], v[176:179], v[184:187], v[136:139]
	s_waitcnt vmcnt(14)
	v_mfma_f32_16x16x32_bf16 v[140:143], v[176:179], v[188:191], v[140:143]
	s_waitcnt vmcnt(13)
	v_mfma_f32_16x16x32_bf16 v[144:147], v[176:179], v[192:195], v[144:147]
	s_waitcnt vmcnt(12)
	v_mfma_f32_16x16x32_bf16 v[160:163], v[176:179], v[196:199], v[160:163]
	s_waitcnt vmcnt(11)
	v_mfma_f32_16x16x32_bf16 v[164:167], v[176:179], v[200:203], v[164:167]
	s_waitcnt vmcnt(10)
	v_mfma_f32_16x16x32_bf16 v[168:171], v[176:179], v[204:207], v[168:171]
	s_waitcnt vmcnt(9)
	v_mfma_f32_16x16x32_bf16 v[128:131], v[176:179], v[208:211], v[128:131]
	global_load_dwordx4 v[176:179], v[126:127], off offset:192
	global_load_dwordx4 v[180:183], v[4:5], off offset:192
	global_load_dwordx4 v[184:187], v[48:49], off
	global_load_dwordx4 v[188:191], v[50:51], off
	global_load_dwordx4 v[192:195], v[52:53], off
	global_load_dwordx4 v[196:199], v[54:55], off
	global_load_dwordx4 v[200:203], v[56:57], off
	global_load_dwordx4 v[204:207], v[58:59], off
	global_load_dwordx4 v[208:211], v[60:61], off
	s_waitcnt vmcnt(16)
	v_mfma_f32_16x16x32_bf16 v[132:135], v[212:215], v[216:219], v[132:135]
	s_waitcnt vmcnt(15)
	v_mfma_f32_16x16x32_bf16 v[136:139], v[212:215], v[220:223], v[136:139]
	s_waitcnt vmcnt(14)
	v_mfma_f32_16x16x32_bf16 v[140:143], v[212:215], v[224:227], v[140:143]
	s_waitcnt vmcnt(13)
	v_mfma_f32_16x16x32_bf16 v[144:147], v[212:215], v[228:231], v[144:147]
	s_waitcnt vmcnt(12)
	v_mfma_f32_16x16x32_bf16 v[160:163], v[212:215], v[232:235], v[160:163]
	s_waitcnt vmcnt(11)
	v_mfma_f32_16x16x32_bf16 v[164:167], v[212:215], v[236:239], v[164:167]
	s_waitcnt vmcnt(10)
	v_mfma_f32_16x16x32_bf16 v[168:171], v[212:215], v[240:243], v[168:171]
	s_waitcnt vmcnt(9)
	v_mfma_f32_16x16x32_bf16 v[128:131], v[212:215], v[244:247], v[128:131]
	s_waitcnt vmcnt(7)
	v_mfma_f32_16x16x32_bf16 v[132:135], v[176:179], v[180:183], v[132:135]
	s_waitcnt vmcnt(6)
	v_mfma_f32_16x16x32_bf16 v[136:139], v[176:179], v[184:187], v[136:139]
	s_waitcnt vmcnt(5)
	v_mfma_f32_16x16x32_bf16 v[140:143], v[176:179], v[188:191], v[140:143]
	s_waitcnt vmcnt(4)
	v_mfma_f32_16x16x32_bf16 v[144:147], v[176:179], v[192:195], v[144:147]
	s_waitcnt vmcnt(3)
	v_mfma_f32_16x16x32_bf16 v[160:163], v[176:179], v[196:199], v[160:163]
	s_waitcnt vmcnt(2)
	v_mfma_f32_16x16x32_bf16 v[164:167], v[176:179], v[200:203], v[164:167]
	s_waitcnt vmcnt(1)
	v_mfma_f32_16x16x32_bf16 v[168:171], v[176:179], v[204:207], v[168:171]
	s_waitcnt vmcnt(0)
; __device__ __forceinline__ void p11_route(Frame& F) {
;     ...
;         for (int c = 0; c < 2; ++c) {
;             f32x4 acc[8];
; #pragma unroll
;             for (int nt = 0; nt < 8; ++nt) acc[nt] = (f32x4){0.f, 0.f, 0.f, 0.f};
; #pragma unroll
;             for (int ks = 0; ks < 4; ++ks) { const gbf16x8 a = *(const gbf16x8*)(QRY + (size_t)(t0 + l15) * 2048 + h * 256 + c * 128 + 32 * ks + 8 * g);
; #pragma unroll
;                 for (int nt = 0; nt < 8; ++nt) acc[nt] = __builtin_amdgcn_mfma_f32_16x16x32_bf16(a, *(const gbf16x8*)(SK + ((size_t)(h * 2 + c) * PNK + 16 * nt + l15) * 128 + 32 * ks + 8 * g), acc[nt], 0, 0, 0); }
; #pragma unroll
;             for (int nt = 0; nt < 8; ++nt)
; #pragma unroll
;                 for (int r = 0; r < 4; ++r) sc[(c * 16 + 4 * g + r) * 129 + 16 * nt + l15] = acc[nt][r];
	v_mfma_f32_16x16x32_bf16 v[128:131], v[176:179], v[208:211], v[128:131]
	s_nop 3
	ds_write2_b32 v151, v132, v136 offset1:16
	ds_write2_b32 v151, v133, v137 offset0:129 offset1:145
	v_add_u32_e32 v132, 0x400, v151
	ds_write2_b32 v132, v134, v138 offset0:2 offset1:18
	ds_write2_b32 v132, v135, v139 offset0:131 offset1:147
	ds_write2_b32 v151, v140, v144 offset0:32 offset1:48
	ds_write2_b32 v151, v141, v145 offset0:161 offset1:177
	ds_write2_b32 v132, v142, v146 offset0:34 offset1:50
	ds_write2_b32 v132, v143, v147 offset0:163 offset1:179
	ds_write2_b32 v151, v160, v164 offset0:64 offset1:80
	ds_write2_b32 v151, v161, v165 offset0:193 offset1:209
	ds_write2_b32 v132, v162, v166 offset0:66 offset1:82
	ds_write2_b32 v132, v163, v167 offset0:195 offset1:211
	ds_write2_b32 v151, v168, v128 offset0:96 offset1:112
	ds_write2_b32 v151, v169, v129 offset0:225 offset1:241
	ds_write2_b32 v132, v170, v130 offset0:98 offset1:114
	ds_write2_b32 v132, v171, v131 offset0:227 offset1:243
	global_load_dwordx4 v[128:131], v[126:127], off offset:256
	global_load_dwordx4 v[132:135], v[62:63], off
	global_load_dwordx4 v[136:139], v[64:65], off
	global_load_dwordx4 v[140:143], v[66:67], off
	global_load_dwordx4 v[144:147], v[68:69], off
	global_load_dwordx4 v[160:163], v[70:71], off
	global_load_dwordx4 v[164:167], v[72:73], off
	global_load_dwordx4 v[168:171], v[74:75], off
	global_load_dwordx4 v[172:175], v[76:77], off
	global_load_dwordx4 v[176:179], v[126:127], off offset:320
	global_load_dwordx4 v[180:183], v[78:79], off
	global_load_dwordx4 v[184:187], v[80:81], off
	global_load_dwordx4 v[188:191], v[82:83], off
	global_load_dwordx4 v[192:195], v[84:85], off
	global_load_dwordx4 v[196:199], v[86:87], off
	global_load_dwordx4 v[200:203], v[88:89], off
	global_load_dwordx4 v[204:207], v[90:91], off
	global_load_dwordx4 v[208:211], v[92:93], off
	global_load_dwordx4 v[212:215], v[126:127], off offset:384
	global_load_dwordx4 v[216:219], v[94:95], off
	global_load_dwordx4 v[220:223], v[96:97], off
	global_load_dwordx4 v[224:227], v[98:99], off
	global_load_dwordx4 v[228:231], v[100:101], off
	global_load_dwordx4 v[232:235], v[102:103], off
	global_load_dwordx4 v[236:239], v[104:105], off
	global_load_dwordx4 v[240:243], v[106:107], off
	global_load_dwordx4 v[244:247], v[108:109], off
	s_waitcnt vmcnt(25)
	v_mfma_f32_16x16x32_bf16 v[132:135], v[128:131], v[132:135], 0
	s_waitcnt vmcnt(24)
	v_mfma_f32_16x16x32_bf16 v[136:139], v[128:131], v[136:139], 0
	s_waitcnt vmcnt(23)
	v_mfma_f32_16x16x32_bf16 v[140:143], v[128:131], v[140:143], 0
	s_waitcnt vmcnt(22)
	v_mfma_f32_16x16x32_bf16 v[144:147], v[128:131], v[144:147], 0
	s_waitcnt vmcnt(21)
	v_mfma_f32_16x16x32_bf16 v[160:163], v[128:131], v[160:163], 0
	s_waitcnt vmcnt(20)
	v_mfma_f32_16x16x32_bf16 v[164:167], v[128:131], v[164:167], 0
	s_waitcnt vmcnt(19)
	v_mfma_f32_16x16x32_bf16 v[168:171], v[128:131], v[168:171], 0
	s_waitcnt vmcnt(18)
	v_mfma_f32_16x16x32_bf16 v[128:131], v[128:131], v[172:175], 0
	s_waitcnt vmcnt(16)
	v_mfma_f32_16x16x32_bf16 v[132:135], v[176:179], v[180:183], v[132:135]
	s_waitcnt vmcnt(15)
	v_mfma_f32_16x16x32_bf16 v[136:139], v[176:179], v[184:187], v[136:139]
	s_waitcnt vmcnt(14)
	v_mfma_f32_16x16x32_bf16 v[140:143], v[176:179], v[188:191], v[140:143]
	s_waitcnt vmcnt(13)
	v_mfma_f32_16x16x32_bf16 v[144:147], v[176:179], v[192:195], v[144:147]
	s_waitcnt vmcnt(12)
	v_mfma_f32_16x16x32_bf16 v[160:163], v[176:179], v[196:199], v[160:163]
	s_waitcnt vmcnt(11)
	v_mfma_f32_16x16x32_bf16 v[164:167], v[176:179], v[200:203], v[164:167]
	s_waitcnt vmcnt(10)
	v_mfma_f32_16x16x32_bf16 v[168:171], v[176:179], v[204:207], v[168:171]
	s_waitcnt vmcnt(9)
	v_mfma_f32_16x16x32_bf16 v[128:131], v[176:179], v[208:211], v[128:131]
	global_load_dwordx4 v[176:179], v[126:127], off offset:448
	global_load_dwordx4 v[180:183], v[110:111], off
	global_load_dwordx4 v[184:187], v[112:113], off
	global_load_dwordx4 v[188:191], v[114:115], off
	global_load_dwordx4 v[192:195], v[116:117], off
	global_load_dwordx4 v[196:199], v[118:119], off
	global_load_dwordx4 v[200:203], v[120:121], off
	global_load_dwordx4 v[204:207], v[122:123], off
	global_load_dwordx4 v[208:211], v[124:125], off
	s_waitcnt vmcnt(16)
	v_mfma_f32_16x16x32_bf16 v[132:135], v[212:215], v[216:219], v[132:135]
	s_waitcnt vmcnt(15)
	v_mfma_f32_16x16x32_bf16 v[136:139], v[212:215], v[220:223], v[136:139]
	s_waitcnt vmcnt(14)
	v_mfma_f32_16x16x32_bf16 v[140:143], v[212:215], v[224:227], v[140:143]
	s_waitcnt vmcnt(13)
	v_mfma_f32_16x16x32_bf16 v[144:147], v[212:215], v[228:231], v[144:147]
	s_waitcnt vmcnt(12)
	v_mfma_f32_16x16x32_bf16 v[160:163], v[212:215], v[232:235], v[160:163]
	s_waitcnt vmcnt(11)
	v_mfma_f32_16x16x32_bf16 v[164:167], v[212:215], v[236:239], v[164:167]
	s_waitcnt vmcnt(10)
	v_mfma_f32_16x16x32_bf16 v[168:171], v[212:215], v[240:243], v[168:171]
	s_waitcnt vmcnt(9)
	v_mfma_f32_16x16x32_bf16 v[128:131], v[212:215], v[244:247], v[128:131]
	s_waitcnt vmcnt(7)
	v_mfma_f32_16x16x32_bf16 v[132:135], v[176:179], v[180:183], v[132:135]
	s_waitcnt vmcnt(6)
	v_mfma_f32_16x16x32_bf16 v[136:139], v[176:179], v[184:187], v[136:139]
	s_waitcnt vmcnt(5)
	v_mfma_f32_16x16x32_bf16 v[140:143], v[176:179], v[188:191], v[140:143]
	s_waitcnt vmcnt(4)
	v_mfma_f32_16x16x32_bf16 v[144:147], v[176:179], v[192:195], v[144:147]
	s_waitcnt vmcnt(3)
	v_mfma_f32_16x16x32_bf16 v[160:163], v[176:179], v[196:199], v[160:163]
	s_waitcnt vmcnt(2)
	v_mfma_f32_16x16x32_bf16 v[164:167], v[176:179], v[200:203], v[164:167]
	s_waitcnt vmcnt(1)
	v_mfma_f32_16x16x32_bf16 v[168:171], v[176:179], v[204:207], v[168:171]
	s_waitcnt vmcnt(0)
; #define LAS __attribute__((address_space(3)))
; __device__ __forceinline__ float uniq_key(float s, int n) { return __uint_as_float((__float_as_uint(s) & ~0xffu) | (unsigned)(255 - n)); }
; #define INS16(A_, X_) do { float x_ = (X_); _Pragma("unroll") for (int i_ = 0; i_ < 16; ++i_) { const float hi_ = fmaxf(A_[i_], x_); x_ = fminf(A_[i_], x_); A_[i_] = hi_; } } while (0)
; __device__ __forceinline__ void p11_route(Frame& F) {
;     ...
;             for (int nt = 0; nt < 8; ++nt)
; #pragma unroll
;                 for (int r = 0; r < 4; ++r) sc[(c * 16 + 4 * g + r) * 129 + 16 * nt + l15] = acc[nt][r];
;         }
;         { LAS float* row = sc + (F.lane & 31) * 129; float a[16]; const int nb = (F.lane >> 5) * (PNK / 2);
; #pragma unroll
;             for (int i = 0; i < 16; ++i) a[i] = -INFINITY;
; #pragma unroll 4
;             for (int n = 0; n < PNK / 2; ++n) INS16(a, uniq_key(row[nb + n], nb + n));
	v_mfma_f32_16x16x32_bf16 v[126:129], v[176:179], v[208:211], v[128:131]
	s_nop 2
	v_add_u32_e32 v130, 0x2000, v151
	v_add_u32_e32 v131, 0x2400, v151
	ds_write2_b32 v130, v132, v136 offset0:16 offset1:32
	ds_write2_b32 v130, v133, v137 offset0:145 offset1:161
	ds_write2_b32 v131, v134, v138 offset0:18 offset1:34
	ds_write2_b32 v131, v135, v139 offset0:147 offset1:163
	ds_write2_b32 v130, v140, v144 offset0:48 offset1:64
	ds_write2_b32 v130, v141, v145 offset0:177 offset1:193
	ds_write2_b32 v131, v142, v146 offset0:50 offset1:66
	ds_write2_b32 v131, v143, v147 offset0:179 offset1:195
	ds_write2_b32 v130, v160, v164 offset0:80 offset1:96
	ds_write2_b32 v130, v161, v165 offset0:209 offset1:225
	ds_write2_b32 v131, v162, v166 offset0:82 offset1:98
	ds_write2_b32 v131, v163, v167 offset0:211 offset1:227
	ds_write2_b32 v130, v168, v126 offset0:112 offset1:128
	v_add_u32_e32 v126, 0x2200, v151
	ds_write2_b32 v126, v169, v127 offset0:113 offset1:129
	ds_write2_b32 v131, v170, v128 offset0:114 offset1:130
	v_add_u32_e32 v126, 0x2600, v151
	ds_write2_b32 v126, v171, v129 offset0:115 offset1:131
	ds_read2_b32 v[222:223], v155 offset0:0 offset1:1
	ds_read2_b32 v[224:225], v155 offset0:2 offset1:3
	ds_read2_b32 v[226:227], v155 offset0:4 offset1:5
	ds_read2_b32 v[228:229], v155 offset0:6 offset1:7
	ds_read2_b32 v[230:231], v155 offset0:8 offset1:9
	ds_read2_b32 v[232:233], v155 offset0:10 offset1:11
	ds_read2_b32 v[234:235], v155 offset0:12 offset1:13
	ds_read2_b32 v[236:237], v155 offset0:14 offset1:15
	s_waitcnt lgkmcnt(0)
	ds_read2_b32 v[238:239], v155 offset0:16 offset1:17
	ds_read2_b32 v[240:241], v155 offset0:18 offset1:19
	ds_read2_b32 v[242:243], v155 offset0:20 offset1:21
	ds_read2_b32 v[244:245], v155 offset0:22 offset1:23
	ds_read2_b32 v[246:247], v155 offset0:24 offset1:25
	ds_read2_b32 v[248:249], v155 offset0:26 offset1:27
	ds_read2_b32 v[250:251], v155 offset0:28 offset1:29
	ds_read2_b32 v[252:253], v155 offset0:30 offset1:31
	v_add_u32_e32 v127, 3, v156
	v_and_or_b32 v222, v222, s14, v127
	v_add_u32_e32 v130, 2, v156
	v_and_or_b32 v223, v223, s14, v130
	v_add_u32_e32 v127, 1, v156
	v_and_or_b32 v224, v224, s14, v127
	v_add_u32_e32 v130, 0, v156
	v_and_or_b32 v225, v225, s14, v130
	v_add_u32_e32 v127, -1, v156
	v_and_or_b32 v226, v226, s14, v127
	v_add_u32_e32 v130, -2, v156
	v_and_or_b32 v227, v227, s14, v130
	v_add_u32_e32 v127, -3, v156
	v_and_or_b32 v228, v228, s14, v127
	v_add_u32_e32 v130, -4, v156
	v_and_or_b32 v229, v229, s14, v130
	v_add_u32_e32 v127, -5, v156
	v_and_or_b32 v230, v230, s14, v127
	v_add_u32_e32 v130, -6, v156
	v_and_or_b32 v231, v231, s14, v130
	v_add_u32_e32 v127, -7, v156
	v_and_or_b32 v232, v232, s14, v127
	v_add_u32_e32 v130, -8, v156
	v_and_or_b32 v233, v233, s14, v130
	v_add_u32_e32 v127, -9, v156
	v_and_or_b32 v234, v234, s14, v127
	v_add_u32_e32 v130, -10, v156
	v_and_or_b32 v235, v235, s14, v130
	v_add_u32_e32 v127, -11, v156
	v_and_or_b32 v236, v236, s14, v127
	v_add_u32_e32 v130, -12, v156
	v_and_or_b32 v237, v237, s14, v130
	v_max_f32_e32 v254, v222, v223
	v_min_f32_e32 v223, v222, v223
	v_max_f32_e32 v222, v224, v225
	v_min_f32_e32 v225, v224, v225
	v_max_f32_e32 v224, v254, v222
	v_min_f32_e32 v222, v254, v222
	v_max_f32_e32 v254, v223, v225
	v_min_f32_e32 v225, v223, v225
	v_max_f32_e32 v223, v254, v222
	v_min_f32_e32 v222, v254, v222
	v_max_f32_e32 v254, v226, v227
	v_min_f32_e32 v227, v226, v227
	v_max_f32_e32 v226, v228, v229
	v_min_f32_e32 v229, v228, v229
	v_max_f32_e32 v228, v254, v226
	v_min_f32_e32 v226, v254, v226
	v_max_f32_e32 v254, v227, v229
	v_min_f32_e32 v229, v227, v229
	v_max_f32_e32 v227, v254, v226
	v_min_f32_e32 v226, v254, v226
	v_max_f32_e32 v254, v224, v228
	v_min_f32_e32 v228, v224, v228
	v_max_f32_e32 v224, v222, v226
	v_min_f32_e32 v226, v222, v226
	v_max_f32_e32 v222, v224, v228
	v_min_f32_e32 v228, v224, v228
	v_max_f32_e32 v224, v223, v227
	v_min_f32_e32 v227, v223, v227
	v_max_f32_e32 v223, v225, v229
	v_min_f32_e32 v229, v225, v229
	v_max_f32_e32 v225, v223, v227
	v_min_f32_e32 v227, v223, v227
	v_max_f32_e32 v223, v224, v222
	v_min_f32_e32 v222, v224, v222
	v_max_f32_e32 v224, v225, v228
	v_min_f32_e32 v228, v225, v228
	v_max_f32_e32 v225, v227, v226
	v_min_f32_e32 v226, v227, v226
	v_max_f32_e32 v227, v230, v231
	v_min_f32_e32 v231, v230, v231
	v_max_f32_e32 v230, v232, v233
	v_min_f32_e32 v233, v232, v233
	v_max_f32_e32 v232, v227, v230
	v_min_f32_e32 v230, v227, v230
	v_max_f32_e32 v227, v231, v233
	v_min_f32_e32 v233, v231, v233
	v_max_f32_e32 v231, v227, v230
	v_min_f32_e32 v230, v227, v230
	v_max_f32_e32 v227, v234, v235
	v_min_f32_e32 v235, v234, v235
	v_max_f32_e32 v234, v236, v237
	v_min_f32_e32 v237, v236, v237
	v_max_f32_e32 v236, v227, v234
	v_min_f32_e32 v234, v227, v234
	v_max_f32_e32 v227, v235, v237
	v_min_f32_e32 v237, v235, v237
	v_max_f32_e32 v235, v227, v234
	v_min_f32_e32 v234, v227, v234
	v_max_f32_e32 v227, v232, v236
	v_min_f32_e32 v236, v232, v236
	v_max_f32_e32 v232, v230, v234
	v_min_f32_e32 v234, v230, v234
	v_max_f32_e32 v230, v232, v236
	v_min_f32_e32 v236, v232, v236
	v_max_f32_e32 v232, v231, v235
	v_min_f32_e32 v235, v231, v235
	v_max_f32_e32 v231, v233, v237
	v_min_f32_e32 v237, v233, v237
	v_max_f32_e32 v233, v231, v235
	v_min_f32_e32 v235, v231, v235
	v_max_f32_e32 v231, v232, v230
	v_min_f32_e32 v230, v232, v230
	v_max_f32_e32 v232, v233, v236
	v_min_f32_e32 v236, v233, v236
	v_max_f32_e32 v233, v235, v234
	v_min_f32_e32 v234, v235, v234
	v_max_f32_e32 v235, v254, v227
	v_min_f32_e32 v227, v254, v227
	v_max_f32_e32 v254, v228, v236
	v_min_f32_e32 v236, v228, v236
	v_max_f32_e32 v228, v254, v227
	v_min_f32_e32 v227, v254, v227
; #define LAS __attribute__((address_space(3)))
; __device__ __forceinline__ float uniq_key(float s, int n) { return __uint_as_float((__float_as_uint(s) & ~0xffu) | (unsigned)(255 - n)); }
; #define INS16(A_, X_) do { float x_ = (X_); _Pragma("unroll") for (int i_ = 0; i_ < 16; ++i_) { const float hi_ = fmaxf(A_[i_], x_); x_ = fminf(A_[i_], x_); A_[i_] = hi_; } } while (0)
; __device__ __forceinline__ void p11_route(Frame& F) {
;     ...
;         { LAS float* row = sc + (F.lane & 31) * 129; float a[16]; const int nb = (F.lane >> 5) * (PNK / 2);
; #pragma unroll
;             for (int i = 0; i < 16; ++i) a[i] = -INFINITY;
; #pragma unroll 4
;             for (int n = 0; n < PNK / 2; ++n) INS16(a, uniq_key(row[nb + n], nb + n));
	v_max_f32_e32 v254, v222, v230
	v_min_f32_e32 v230, v222, v230
	v_max_f32_e32 v222, v226, v234
	v_min_f32_e32 v234, v226, v234
	v_max_f32_e32 v226, v222, v230
	v_min_f32_e32 v230, v222, v230
	v_max_f32_e32 v222, v254, v228
	v_min_f32_e32 v228, v254, v228
	v_max_f32_e32 v254, v226, v227
	v_min_f32_e32 v227, v226, v227
	v_max_f32_e32 v226, v230, v236
	v_min_f32_e32 v236, v230, v236
	v_max_f32_e32 v230, v223, v231
	v_min_f32_e32 v231, v223, v231
	v_max_f32_e32 v223, v225, v233
	v_min_f32_e32 v233, v225, v233
	v_max_f32_e32 v225, v223, v231
	v_min_f32_e32 v231, v223, v231
	v_max_f32_e32 v223, v224, v232
	v_min_f32_e32 v232, v224, v232
	v_max_f32_e32 v224, v229, v237
	v_min_f32_e32 v237, v229, v237
	v_max_f32_e32 v229, v224, v232
	v_min_f32_e32 v232, v224, v232
	v_max_f32_e32 v224, v223, v225
	v_min_f32_e32 v225, v223, v225
	v_max_f32_e32 v223, v229, v231
	v_min_f32_e32 v231, v229, v231
	v_max_f32_e32 v229, v232, v233
	v_min_f32_e32 v233, v232, v233
	v_max_f32_e32 v232, v230, v222
	v_min_f32_e32 v222, v230, v222
	v_max_f32_e32 v230, v224, v228
	v_min_f32_e32 v228, v224, v228
	v_max_f32_e32 v224, v225, v254
	v_min_f32_e32 v254, v225, v254
	v_max_f32_e32 v225, v223, v227
	v_min_f32_e32 v227, v223, v227
	v_max_f32_e32 v223, v231, v226
	v_min_f32_e32 v226, v231, v226
	v_max_f32_e32 v231, v229, v236
	v_min_f32_e32 v236, v229, v236
	v_max_f32_e32 v229, v233, v234
	v_min_f32_e32 v234, v233, v234
	s_waitcnt lgkmcnt(0)
	v_add_u32_e32 v127, -13, v156
	v_and_or_b32 v238, v238, s14, v127
	v_add_u32_e32 v130, -14, v156
	v_and_or_b32 v239, v239, s14, v130
	v_add_u32_e32 v127, -15, v156
	v_and_or_b32 v240, v240, s14, v127
	v_add_u32_e32 v130, -16, v156
	v_and_or_b32 v241, v241, s14, v130
	v_add_u32_e32 v127, 0xffffffef, v156
	v_and_or_b32 v242, v242, s14, v127
	v_add_u32_e32 v130, 0xffffffee, v156
	v_and_or_b32 v243, v243, s14, v130
	v_add_u32_e32 v127, 0xffffffed, v156
	v_and_or_b32 v244, v244, s14, v127
	v_add_u32_e32 v130, 0xffffffec, v156
	v_and_or_b32 v245, v245, s14, v130
	v_add_u32_e32 v127, 0xffffffeb, v156
	v_and_or_b32 v246, v246, s14, v127
	v_add_u32_e32 v130, 0xffffffea, v156
	v_and_or_b32 v247, v247, s14, v130
	v_add_u32_e32 v127, 0xffffffe9, v156
	v_and_or_b32 v248, v248, s14, v127
	v_add_u32_e32 v130, 0xffffffe8, v156
	v_and_or_b32 v249, v249, s14, v130
	v_add_u32_e32 v127, 0xffffffe7, v156
	v_and_or_b32 v250, v250, s14, v127
	v_add_u32_e32 v130, 0xffffffe6, v156
	v_and_or_b32 v251, v251, s14, v130
	v_add_u32_e32 v127, 0xffffffe5, v156
	v_and_or_b32 v252, v252, s14, v127
	v_add_u32_e32 v130, 0xffffffe4, v156
	v_and_or_b32 v253, v253, s14, v130
	v_max_f32_e32 v128, v238, v239
	v_min_f32_e32 v239, v238, v239
	v_max_f32_e32 v238, v240, v241
	v_min_f32_e32 v241, v240, v241
	v_max_f32_e32 v240, v128, v238
	v_min_f32_e32 v238, v128, v238
	v_max_f32_e32 v128, v239, v241
	v_min_f32_e32 v241, v239, v241
	v_max_f32_e32 v239, v128, v238
	v_min_f32_e32 v238, v128, v238
	v_max_f32_e32 v128, v242, v243
	v_min_f32_e32 v243, v242, v243
	v_max_f32_e32 v242, v244, v245
	v_min_f32_e32 v245, v244, v245
	v_max_f32_e32 v244, v128, v242
	v_min_f32_e32 v242, v128, v242
	v_max_f32_e32 v128, v243, v245
	v_min_f32_e32 v245, v243, v245
	v_max_f32_e32 v243, v128, v242
	v_min_f32_e32 v242, v128, v242
	v_max_f32_e32 v128, v240, v244
	v_min_f32_e32 v244, v240, v244
	v_max_f32_e32 v240, v238, v242
	v_min_f32_e32 v242, v238, v242
	v_max_f32_e32 v238, v240, v244
	v_min_f32_e32 v244, v240, v244
	v_max_f32_e32 v240, v239, v243
	v_min_f32_e32 v243, v239, v243
	v_max_f32_e32 v239, v241, v245
	v_min_f32_e32 v245, v241, v245
	v_max_f32_e32 v241, v239, v243
	v_min_f32_e32 v243, v239, v243
	v_max_f32_e32 v239, v240, v238
	v_min_f32_e32 v238, v240, v238
	v_max_f32_e32 v240, v241, v244
	v_min_f32_e32 v244, v241, v244
	v_max_f32_e32 v241, v243, v242
	v_min_f32_e32 v242, v243, v242
	v_max_f32_e32 v243, v246, v247
	v_min_f32_e32 v247, v246, v247
	v_max_f32_e32 v246, v248, v249
	v_min_f32_e32 v249, v248, v249
	v_max_f32_e32 v248, v243, v246
	v_min_f32_e32 v246, v243, v246
	v_max_f32_e32 v243, v247, v249
	v_min_f32_e32 v249, v247, v249
	v_max_f32_e32 v247, v243, v246
	v_min_f32_e32 v246, v243, v246
	v_max_f32_e32 v243, v250, v251
	v_min_f32_e32 v251, v250, v251
	v_max_f32_e32 v250, v252, v253
	v_min_f32_e32 v253, v252, v253
	v_max_f32_e32 v252, v243, v250
	v_min_f32_e32 v250, v243, v250
	v_max_f32_e32 v243, v251, v253
	v_min_f32_e32 v253, v251, v253
	v_max_f32_e32 v251, v243, v250
	v_min_f32_e32 v250, v243, v250
	v_max_f32_e32 v243, v248, v252
	v_min_f32_e32 v252, v248, v252
	v_max_f32_e32 v248, v246, v250
	v_min_f32_e32 v250, v246, v250
	v_max_f32_e32 v246, v248, v252
	v_min_f32_e32 v252, v248, v252
	v_max_f32_e32 v248, v247, v251
	v_min_f32_e32 v251, v247, v251
	v_max_f32_e32 v247, v249, v253
	v_min_f32_e32 v253, v249, v253
	v_max_f32_e32 v249, v247, v251
	v_min_f32_e32 v251, v247, v251
	v_max_f32_e32 v247, v248, v246
	v_min_f32_e32 v246, v248, v246
	v_max_f32_e32 v248, v249, v252
	v_min_f32_e32 v252, v249, v252
	v_max_f32_e32 v249, v251, v250
	v_min_f32_e32 v250, v251, v250
	v_max_f32_e32 v251, v128, v243
	v_min_f32_e32 v243, v128, v243
	v_max_f32_e32 v128, v244, v252
	v_min_f32_e32 v252, v244, v252
	v_max_f32_e32 v244, v128, v243
	v_min_f32_e32 v243, v128, v243
	v_max_f32_e32 v128, v238, v246
	v_min_f32_e32 v246, v238, v246
	v_max_f32_e32 v238, v242, v250
	v_min_f32_e32 v250, v242, v250
	v_max_f32_e32 v242, v238, v246
	v_min_f32_e32 v246, v238, v246
	v_max_f32_e32 v238, v128, v244
	v_min_f32_e32 v244, v128, v244
	v_max_f32_e32 v128, v242, v243
	v_min_f32_e32 v243, v242, v243
	v_max_f32_e32 v242, v246, v252
	v_min_f32_e32 v252, v246, v252
	v_max_f32_e32 v246, v239, v247
; #define LAS __attribute__((address_space(3)))
; __device__ __forceinline__ float uniq_key(float s, int n) { return __uint_as_float((__float_as_uint(s) & ~0xffu) | (unsigned)(255 - n)); }
; #define INS16(A_, X_) do { float x_ = (X_); _Pragma("unroll") for (int i_ = 0; i_ < 16; ++i_) { const float hi_ = fmaxf(A_[i_], x_); x_ = fminf(A_[i_], x_); A_[i_] = hi_; } } while (0)
; __device__ __forceinline__ void p11_route(Frame& F) {
;     ...
;         { LAS float* row = sc + (F.lane & 31) * 129; float a[16]; const int nb = (F.lane >> 5) * (PNK / 2);
; #pragma unroll
;             for (int i = 0; i < 16; ++i) a[i] = -INFINITY;
; #pragma unroll 4
;             for (int n = 0; n < PNK / 2; ++n) INS16(a, uniq_key(row[nb + n], nb + n));
	v_min_f32_e32 v247, v239, v247
	v_max_f32_e32 v239, v241, v249
	v_min_f32_e32 v249, v241, v249
	v_max_f32_e32 v241, v239, v247
	v_min_f32_e32 v247, v239, v247
	v_max_f32_e32 v239, v240, v248
	v_min_f32_e32 v248, v240, v248
	v_max_f32_e32 v240, v245, v253
	v_min_f32_e32 v253, v245, v253
	v_max_f32_e32 v245, v240, v248
	v_min_f32_e32 v248, v240, v248
	v_max_f32_e32 v240, v239, v241
	v_min_f32_e32 v241, v239, v241
	v_max_f32_e32 v239, v245, v247
	v_min_f32_e32 v247, v245, v247
	v_max_f32_e32 v245, v248, v249
	v_min_f32_e32 v249, v248, v249
	v_max_f32_e32 v248, v246, v238
	v_min_f32_e32 v238, v246, v238
	v_max_f32_e32 v246, v240, v244
	v_min_f32_e32 v244, v240, v244
	v_max_f32_e32 v240, v241, v128
	v_min_f32_e32 v128, v241, v128
	v_max_f32_e32 v241, v239, v243
	v_min_f32_e32 v243, v239, v243
	v_max_f32_e32 v239, v247, v242
	v_min_f32_e32 v242, v247, v242
	v_max_f32_e32 v247, v245, v252
	v_min_f32_e32 v252, v245, v252
	v_max_f32_e32 v245, v249, v250
	v_min_f32_e32 v250, v249, v250
	v_max_f32_e32 v235, v235, v253
	v_max_f32_e32 v232, v232, v250
	v_max_f32_e32 v222, v222, v245
	v_max_f32_e32 v230, v230, v252
	v_max_f32_e32 v228, v228, v247
	v_max_f32_e32 v224, v224, v242
	v_max_f32_e32 v254, v254, v239
	v_max_f32_e32 v225, v225, v243
	v_max_f32_e32 v227, v227, v241
	v_max_f32_e32 v223, v223, v128
	v_max_f32_e32 v226, v226, v240
	v_max_f32_e32 v231, v231, v244
	v_max_f32_e32 v236, v236, v246
	v_max_f32_e32 v229, v229, v238
	v_max_f32_e32 v234, v234, v248
	v_max_f32_e32 v237, v237, v251
	ds_read2_b32 v[238:239], v155 offset0:32 offset1:33
	ds_read2_b32 v[240:241], v155 offset0:34 offset1:35
	ds_read2_b32 v[242:243], v155 offset0:36 offset1:37
	ds_read2_b32 v[244:245], v155 offset0:38 offset1:39
	ds_read2_b32 v[246:247], v155 offset0:40 offset1:41
	ds_read2_b32 v[248:249], v155 offset0:42 offset1:43
	ds_read2_b32 v[250:251], v155 offset0:44 offset1:45
	ds_read2_b32 v[252:253], v155 offset0:46 offset1:47
	v_max_f32_e32 v233, v235, v227
	v_min_f32_e32 v227, v235, v227
	v_max_f32_e32 v235, v232, v223
	v_min_f32_e32 v223, v232, v223
	v_max_f32_e32 v232, v222, v226
	v_min_f32_e32 v226, v222, v226
	v_max_f32_e32 v222, v230, v231
	v_min_f32_e32 v231, v230, v231
	v_max_f32_e32 v230, v228, v236
	v_min_f32_e32 v236, v228, v236
	v_max_f32_e32 v228, v224, v229
	v_min_f32_e32 v229, v224, v229
	v_max_f32_e32 v224, v254, v234
	v_min_f32_e32 v234, v254, v234
	v_max_f32_e32 v254, v225, v237
	v_min_f32_e32 v237, v225, v237
	v_max_f32_e32 v225, v233, v230
	v_min_f32_e32 v230, v233, v230
	v_max_f32_e32 v233, v235, v228
	v_min_f32_e32 v228, v235, v228
	v_max_f32_e32 v235, v232, v224
	v_min_f32_e32 v224, v232, v224
	v_max_f32_e32 v232, v222, v254
	v_min_f32_e32 v254, v222, v254
	v_max_f32_e32 v222, v227, v236
	v_min_f32_e32 v236, v227, v236
	v_max_f32_e32 v227, v223, v229
	v_min_f32_e32 v229, v223, v229
	v_max_f32_e32 v223, v226, v234
	v_min_f32_e32 v234, v226, v234
	v_max_f32_e32 v226, v231, v237
	v_min_f32_e32 v237, v231, v237
	v_max_f32_e32 v231, v225, v235
	v_min_f32_e32 v235, v225, v235
	v_max_f32_e32 v225, v233, v232
	v_min_f32_e32 v232, v233, v232
	v_max_f32_e32 v233, v230, v224
	v_min_f32_e32 v224, v230, v224
	v_max_f32_e32 v230, v228, v254
	v_min_f32_e32 v254, v228, v254
	v_max_f32_e32 v228, v222, v223
	v_min_f32_e32 v223, v222, v223
	v_max_f32_e32 v222, v227, v226
	v_min_f32_e32 v226, v227, v226
	v_max_f32_e32 v227, v236, v234
	v_min_f32_e32 v234, v236, v234
	v_max_f32_e32 v236, v229, v237
	v_min_f32_e32 v237, v229, v237
	v_max_f32_e32 v229, v231, v225
	v_min_f32_e32 v225, v231, v225
	v_max_f32_e32 v231, v235, v232
	v_min_f32_e32 v232, v235, v232
	v_max_f32_e32 v235, v233, v230
	v_min_f32_e32 v230, v233, v230
	v_max_f32_e32 v233, v224, v254
	v_min_f32_e32 v254, v224, v254
	v_max_f32_e32 v224, v228, v222
	v_min_f32_e32 v222, v228, v222
	v_max_f32_e32 v228, v223, v226
	v_min_f32_e32 v226, v223, v226
	v_max_f32_e32 v223, v227, v236
	v_min_f32_e32 v236, v227, v236
	v_max_f32_e32 v227, v234, v237
	v_min_f32_e32 v237, v234, v237
	s_waitcnt lgkmcnt(0)
	v_add_u32_e32 v127, 0xffffffe3, v156
	v_and_or_b32 v238, v238, s14, v127
	v_add_u32_e32 v130, 0xffffffe2, v156
	v_and_or_b32 v239, v239, s14, v130
	v_add_u32_e32 v127, 0xffffffe1, v156
	v_and_or_b32 v240, v240, s14, v127
	v_add_u32_e32 v130, 0xffffffe0, v156
	v_and_or_b32 v241, v241, s14, v130
	v_add_u32_e32 v127, 0xffffffdf, v156
	v_and_or_b32 v242, v242, s14, v127
	v_add_u32_e32 v130, 0xffffffde, v156
	v_and_or_b32 v243, v243, s14, v130
	v_add_u32_e32 v127, 0xffffffdd, v156
	v_and_or_b32 v244, v244, s14, v127
	v_add_u32_e32 v130, 0xffffffdc, v156
	v_and_or_b32 v245, v245, s14, v130
	v_add_u32_e32 v127, 0xffffffdb, v156
	v_and_or_b32 v246, v246, s14, v127
	v_add_u32_e32 v130, 0xffffffda, v156
	v_and_or_b32 v247, v247, s14, v130
	v_add_u32_e32 v127, 0xffffffd9, v156
	v_and_or_b32 v248, v248, s14, v127
	v_add_u32_e32 v130, 0xffffffd8, v156
	v_and_or_b32 v249, v249, s14, v130
	v_add_u32_e32 v127, 0xffffffd7, v156
	v_and_or_b32 v250, v250, s14, v127
	v_add_u32_e32 v130, 0xffffffd6, v156
	v_and_or_b32 v251, v251, s14, v130
	v_add_u32_e32 v127, 0xffffffd5, v156
	v_and_or_b32 v252, v252, s14, v127
	v_add_u32_e32 v130, 0xffffffd4, v156
	v_and_or_b32 v253, v253, s14, v130
	v_max_f32_e32 v128, v238, v239
	v_min_f32_e32 v239, v238, v239
	v_max_f32_e32 v238, v240, v241
	v_min_f32_e32 v241, v240, v241
	v_max_f32_e32 v240, v128, v238
	v_min_f32_e32 v238, v128, v238
	v_max_f32_e32 v128, v239, v241
	v_min_f32_e32 v241, v239, v241
	v_max_f32_e32 v239, v128, v238
	v_min_f32_e32 v238, v128, v238
	v_max_f32_e32 v128, v242, v243
	v_min_f32_e32 v243, v242, v243
	v_max_f32_e32 v242, v244, v245
	v_min_f32_e32 v245, v244, v245
; #define LAS __attribute__((address_space(3)))
; __device__ __forceinline__ float uniq_key(float s, int n) { return __uint_as_float((__float_as_uint(s) & ~0xffu) | (unsigned)(255 - n)); }
; #define INS16(A_, X_) do { float x_ = (X_); _Pragma("unroll") for (int i_ = 0; i_ < 16; ++i_) { const float hi_ = fmaxf(A_[i_], x_); x_ = fminf(A_[i_], x_); A_[i_] = hi_; } } while (0)
; __device__ __forceinline__ void p11_route(Frame& F) {
;     ...
;         { LAS float* row = sc + (F.lane & 31) * 129; float a[16]; const int nb = (F.lane >> 5) * (PNK / 2);
; #pragma unroll
;             for (int i = 0; i < 16; ++i) a[i] = -INFINITY;
; #pragma unroll 4
;             for (int n = 0; n < PNK / 2; ++n) INS16(a, uniq_key(row[nb + n], nb + n));
	v_max_f32_e32 v244, v128, v242
	v_min_f32_e32 v242, v128, v242
	v_max_f32_e32 v128, v243, v245
	v_min_f32_e32 v245, v243, v245
	v_max_f32_e32 v243, v128, v242
	v_min_f32_e32 v242, v128, v242
	v_max_f32_e32 v128, v240, v244
	v_min_f32_e32 v244, v240, v244
	v_max_f32_e32 v240, v238, v242
	v_min_f32_e32 v242, v238, v242
	v_max_f32_e32 v238, v240, v244
	v_min_f32_e32 v244, v240, v244
	v_max_f32_e32 v240, v239, v243
	v_min_f32_e32 v243, v239, v243
	v_max_f32_e32 v239, v241, v245
	v_min_f32_e32 v245, v241, v245
	v_max_f32_e32 v241, v239, v243
	v_min_f32_e32 v243, v239, v243
	v_max_f32_e32 v239, v240, v238
	v_min_f32_e32 v238, v240, v238
	v_max_f32_e32 v240, v241, v244
	v_min_f32_e32 v244, v241, v244
	v_max_f32_e32 v241, v243, v242
	v_min_f32_e32 v242, v243, v242
	v_max_f32_e32 v243, v246, v247
	v_min_f32_e32 v247, v246, v247
	v_max_f32_e32 v246, v248, v249
	v_min_f32_e32 v249, v248, v249
	v_max_f32_e32 v248, v243, v246
	v_min_f32_e32 v246, v243, v246
	v_max_f32_e32 v243, v247, v249
	v_min_f32_e32 v249, v247, v249
	v_max_f32_e32 v247, v243, v246
	v_min_f32_e32 v246, v243, v246
	v_max_f32_e32 v243, v250, v251
	v_min_f32_e32 v251, v250, v251
	v_max_f32_e32 v250, v252, v253
	v_min_f32_e32 v253, v252, v253
	v_max_f32_e32 v252, v243, v250
	v_min_f32_e32 v250, v243, v250
	v_max_f32_e32 v243, v251, v253
	v_min_f32_e32 v253, v251, v253
	v_max_f32_e32 v251, v243, v250
	v_min_f32_e32 v250, v243, v250
	v_max_f32_e32 v243, v248, v252
	v_min_f32_e32 v252, v248, v252
	v_max_f32_e32 v248, v246, v250
	v_min_f32_e32 v250, v246, v250
	v_max_f32_e32 v246, v248, v252
	v_min_f32_e32 v252, v248, v252
	v_max_f32_e32 v248, v247, v251
	v_min_f32_e32 v251, v247, v251
	v_max_f32_e32 v247, v249, v253
	v_min_f32_e32 v253, v249, v253
	v_max_f32_e32 v249, v247, v251
	v_min_f32_e32 v251, v247, v251
	v_max_f32_e32 v247, v248, v246
	v_min_f32_e32 v246, v248, v246
	v_max_f32_e32 v248, v249, v252
	v_min_f32_e32 v252, v249, v252
	v_max_f32_e32 v249, v251, v250
	v_min_f32_e32 v250, v251, v250
	v_max_f32_e32 v251, v128, v243
	v_min_f32_e32 v243, v128, v243
	v_max_f32_e32 v128, v244, v252
	v_min_f32_e32 v252, v244, v252
	v_max_f32_e32 v244, v128, v243
	v_min_f32_e32 v243, v128, v243
	v_max_f32_e32 v128, v238, v246
	v_min_f32_e32 v246, v238, v246
	v_max_f32_e32 v238, v242, v250
	v_min_f32_e32 v250, v242, v250
	v_max_f32_e32 v242, v238, v246
	v_min_f32_e32 v246, v238, v246
	v_max_f32_e32 v238, v128, v244
	v_min_f32_e32 v244, v128, v244
	v_max_f32_e32 v128, v242, v243
	v_min_f32_e32 v243, v242, v243
	v_max_f32_e32 v242, v246, v252
	v_min_f32_e32 v252, v246, v252
	v_max_f32_e32 v246, v239, v247
	v_min_f32_e32 v247, v239, v247
	v_max_f32_e32 v239, v241, v249
	v_min_f32_e32 v249, v241, v249
	v_max_f32_e32 v241, v239, v247
	v_min_f32_e32 v247, v239, v247
	v_max_f32_e32 v239, v240, v248
	v_min_f32_e32 v248, v240, v248
	v_max_f32_e32 v240, v245, v253
	v_min_f32_e32 v253, v245, v253
	v_max_f32_e32 v245, v240, v248
	v_min_f32_e32 v248, v240, v248
	v_max_f32_e32 v240, v239, v241
	v_min_f32_e32 v241, v239, v241
	v_max_f32_e32 v239, v245, v247
	v_min_f32_e32 v247, v245, v247
	v_max_f32_e32 v245, v248, v249
	v_min_f32_e32 v249, v248, v249
	v_max_f32_e32 v248, v246, v238
	v_min_f32_e32 v238, v246, v238
	v_max_f32_e32 v246, v240, v244
	v_min_f32_e32 v244, v240, v244
	v_max_f32_e32 v240, v241, v128
	v_min_f32_e32 v128, v241, v128
	v_max_f32_e32 v241, v239, v243
	v_min_f32_e32 v243, v239, v243
	v_max_f32_e32 v239, v247, v242
	v_min_f32_e32 v242, v247, v242
	v_max_f32_e32 v247, v245, v252
	v_min_f32_e32 v252, v245, v252
	v_max_f32_e32 v245, v249, v250
	v_min_f32_e32 v250, v249, v250
	v_max_f32_e32 v229, v229, v253
	v_max_f32_e32 v225, v225, v250
	v_max_f32_e32 v231, v231, v245
	v_max_f32_e32 v232, v232, v252
	v_max_f32_e32 v235, v235, v247
	v_max_f32_e32 v230, v230, v242
	v_max_f32_e32 v233, v233, v239
	v_max_f32_e32 v254, v254, v243
	v_max_f32_e32 v224, v224, v241
	v_max_f32_e32 v222, v222, v128
	v_max_f32_e32 v228, v228, v240
	v_max_f32_e32 v226, v226, v244
	v_max_f32_e32 v223, v223, v246
	v_max_f32_e32 v236, v236, v238
	v_max_f32_e32 v227, v227, v248
	v_max_f32_e32 v237, v237, v251
	ds_read2_b32 v[238:239], v155 offset0:48 offset1:49
	ds_read2_b32 v[240:241], v155 offset0:50 offset1:51
	ds_read2_b32 v[242:243], v155 offset0:52 offset1:53
	ds_read2_b32 v[244:245], v155 offset0:54 offset1:55
	ds_read2_b32 v[246:247], v155 offset0:56 offset1:57
	ds_read2_b32 v[248:249], v155 offset0:58 offset1:59
	ds_read2_b32 v[250:251], v155 offset0:60 offset1:61
	ds_read2_b32 v[252:253], v155 offset0:62 offset1:63
	v_max_f32_e32 v234, v229, v224
	v_min_f32_e32 v224, v229, v224
	v_max_f32_e32 v229, v225, v222
	v_min_f32_e32 v222, v225, v222
	v_max_f32_e32 v225, v231, v228
	v_min_f32_e32 v228, v231, v228
	v_max_f32_e32 v231, v232, v226
	v_min_f32_e32 v226, v232, v226
	v_max_f32_e32 v232, v235, v223
	v_min_f32_e32 v223, v235, v223
	v_max_f32_e32 v235, v230, v236
	v_min_f32_e32 v236, v230, v236
	v_max_f32_e32 v230, v233, v227
	v_min_f32_e32 v227, v233, v227
	v_max_f32_e32 v233, v254, v237
	v_min_f32_e32 v237, v254, v237
	v_max_f32_e32 v254, v234, v232
	v_min_f32_e32 v232, v234, v232
	v_max_f32_e32 v234, v229, v235
	v_min_f32_e32 v235, v229, v235
	v_max_f32_e32 v229, v225, v230
	v_min_f32_e32 v230, v225, v230
	v_max_f32_e32 v225, v231, v233
	v_min_f32_e32 v233, v231, v233
	v_max_f32_e32 v231, v224, v223
	v_min_f32_e32 v223, v224, v223
	v_max_f32_e32 v224, v222, v236
	v_min_f32_e32 v236, v222, v236
	v_max_f32_e32 v222, v228, v227
	v_min_f32_e32 v227, v228, v227
	v_max_f32_e32 v228, v226, v237
	v_min_f32_e32 v237, v226, v237
	v_max_f32_e32 v226, v254, v229
	v_min_f32_e32 v229, v254, v229
	v_max_f32_e32 v254, v234, v225
	v_min_f32_e32 v225, v234, v225
	v_max_f32_e32 v234, v232, v230
	v_min_f32_e32 v230, v232, v230
	v_max_f32_e32 v232, v235, v233
	v_min_f32_e32 v233, v235, v233
	v_max_f32_e32 v235, v231, v222
	v_min_f32_e32 v222, v231, v222
	v_max_f32_e32 v231, v224, v228
	v_min_f32_e32 v228, v224, v228
	v_max_f32_e32 v224, v223, v227
	v_min_f32_e32 v227, v223, v227
	v_max_f32_e32 v223, v236, v237
	v_min_f32_e32 v237, v236, v237
	v_max_f32_e32 v236, v226, v254
	v_min_f32_e32 v254, v226, v254
	v_max_f32_e32 v226, v229, v225
	v_min_f32_e32 v225, v229, v225
	v_max_f32_e32 v229, v234, v232
	v_min_f32_e32 v232, v234, v232
	v_max_f32_e32 v234, v230, v233
	v_min_f32_e32 v233, v230, v233
	v_max_f32_e32 v230, v235, v231
	v_min_f32_e32 v231, v235, v231
	v_max_f32_e32 v235, v222, v228
	v_min_f32_e32 v228, v222, v228
	v_max_f32_e32 v222, v224, v223
	v_min_f32_e32 v223, v224, v223
	v_max_f32_e32 v224, v227, v237
	v_min_f32_e32 v237, v227, v237
	s_waitcnt lgkmcnt(0)
; #define LAS __attribute__((address_space(3)))
; __device__ __forceinline__ float uniq_key(float s, int n) { return __uint_as_float((__float_as_uint(s) & ~0xffu) | (unsigned)(255 - n)); }
; #define INS16(A_, X_) do { float x_ = (X_); _Pragma("unroll") for (int i_ = 0; i_ < 16; ++i_) { const float hi_ = fmaxf(A_[i_], x_); x_ = fminf(A_[i_], x_); A_[i_] = hi_; } } while (0)
; __device__ __forceinline__ void p11_route(Frame& F) {
;     ...
;         { LAS float* row = sc + (F.lane & 31) * 129; float a[16]; const int nb = (F.lane >> 5) * (PNK / 2);
; #pragma unroll
;             for (int i = 0; i < 16; ++i) a[i] = -INFINITY;
; #pragma unroll 4
;             for (int n = 0; n < PNK / 2; ++n) INS16(a, uniq_key(row[nb + n], nb + n));
	v_add_u32_e32 v127, 0xffffffd3, v156
	v_and_or_b32 v238, v238, s14, v127
	v_add_u32_e32 v130, 0xffffffd2, v156
	v_and_or_b32 v239, v239, s14, v130
	v_add_u32_e32 v127, 0xffffffd1, v156
	v_and_or_b32 v240, v240, s14, v127
	v_add_u32_e32 v130, 0xffffffd0, v156
	v_and_or_b32 v241, v241, s14, v130
	v_add_u32_e32 v127, 0xffffffcf, v156
	v_and_or_b32 v242, v242, s14, v127
	v_add_u32_e32 v130, 0xffffffce, v156
	v_and_or_b32 v243, v243, s14, v130
	v_add_u32_e32 v127, 0xffffffcd, v156
	v_and_or_b32 v244, v244, s14, v127
	v_add_u32_e32 v130, 0xffffffcc, v156
	v_and_or_b32 v245, v245, s14, v130
	v_add_u32_e32 v127, 0xffffffcb, v156
	v_and_or_b32 v246, v246, s14, v127
	v_add_u32_e32 v130, 0xffffffca, v156
	v_and_or_b32 v247, v247, s14, v130
	v_add_u32_e32 v127, 0xffffffc9, v156
	v_and_or_b32 v248, v248, s14, v127
	v_add_u32_e32 v130, 0xffffffc8, v156
	v_and_or_b32 v249, v249, s14, v130
	v_add_u32_e32 v127, 0xffffffc7, v156
	v_and_or_b32 v250, v250, s14, v127
	v_add_u32_e32 v130, 0xffffffc6, v156
	v_and_or_b32 v251, v251, s14, v130
	v_add_u32_e32 v127, 0xffffffc5, v156
	v_and_or_b32 v252, v252, s14, v127
	v_add_u32_e32 v130, 0xffffffc4, v156
	v_and_or_b32 v253, v253, s14, v130
	v_max_f32_e32 v128, v238, v239
	v_min_f32_e32 v239, v238, v239
	v_max_f32_e32 v238, v240, v241
	v_min_f32_e32 v241, v240, v241
	v_max_f32_e32 v240, v128, v238
	v_min_f32_e32 v238, v128, v238
	v_max_f32_e32 v128, v239, v241
	v_min_f32_e32 v241, v239, v241
	v_max_f32_e32 v239, v128, v238
	v_min_f32_e32 v238, v128, v238
	v_max_f32_e32 v128, v242, v243
	v_min_f32_e32 v243, v242, v243
	v_max_f32_e32 v242, v244, v245
	v_min_f32_e32 v245, v244, v245
	v_max_f32_e32 v244, v128, v242
	v_min_f32_e32 v242, v128, v242
	v_max_f32_e32 v128, v243, v245
	v_min_f32_e32 v245, v243, v245
	v_max_f32_e32 v243, v128, v242
	v_min_f32_e32 v242, v128, v242
	v_max_f32_e32 v128, v240, v244
	v_min_f32_e32 v244, v240, v244
	v_max_f32_e32 v240, v238, v242
	v_min_f32_e32 v242, v238, v242
	v_max_f32_e32 v238, v240, v244
	v_min_f32_e32 v244, v240, v244
	v_max_f32_e32 v240, v239, v243
	v_min_f32_e32 v243, v239, v243
	v_max_f32_e32 v239, v241, v245
	v_min_f32_e32 v245, v241, v245
	v_max_f32_e32 v241, v239, v243
	v_min_f32_e32 v243, v239, v243
	v_max_f32_e32 v239, v240, v238
	v_min_f32_e32 v238, v240, v238
	v_max_f32_e32 v240, v241, v244
	v_min_f32_e32 v244, v241, v244
	v_max_f32_e32 v241, v243, v242
	v_min_f32_e32 v242, v243, v242
	v_max_f32_e32 v243, v246, v247
	v_min_f32_e32 v247, v246, v247
	v_max_f32_e32 v246, v248, v249
	v_min_f32_e32 v249, v248, v249
	v_max_f32_e32 v248, v243, v246
	v_min_f32_e32 v246, v243, v246
	v_max_f32_e32 v243, v247, v249
	v_min_f32_e32 v249, v247, v249
	v_max_f32_e32 v247, v243, v246
	v_min_f32_e32 v246, v243, v246
	v_max_f32_e32 v243, v250, v251
	v_min_f32_e32 v251, v250, v251
	v_max_f32_e32 v250, v252, v253
	v_min_f32_e32 v253, v252, v253
	v_max_f32_e32 v252, v243, v250
	v_min_f32_e32 v250, v243, v250
	v_max_f32_e32 v243, v251, v253
	v_min_f32_e32 v253, v251, v253
	v_max_f32_e32 v251, v243, v250
	v_min_f32_e32 v250, v243, v250
	v_max_f32_e32 v243, v248, v252
	v_min_f32_e32 v252, v248, v252
	v_max_f32_e32 v248, v246, v250
	v_min_f32_e32 v250, v246, v250
	v_max_f32_e32 v246, v248, v252
	v_min_f32_e32 v252, v248, v252
	v_max_f32_e32 v248, v247, v251
	v_min_f32_e32 v251, v247, v251
	v_max_f32_e32 v247, v249, v253
	v_min_f32_e32 v253, v249, v253
	v_max_f32_e32 v249, v247, v251
	v_min_f32_e32 v251, v247, v251
	v_max_f32_e32 v247, v248, v246
	v_min_f32_e32 v246, v248, v246
	v_max_f32_e32 v248, v249, v252
	v_min_f32_e32 v252, v249, v252
	v_max_f32_e32 v249, v251, v250
	v_min_f32_e32 v250, v251, v250
	v_max_f32_e32 v251, v128, v243
	v_min_f32_e32 v243, v128, v243
	v_max_f32_e32 v128, v244, v252
	v_min_f32_e32 v252, v244, v252
	v_max_f32_e32 v244, v128, v243
	v_min_f32_e32 v243, v128, v243
	v_max_f32_e32 v128, v238, v246
	v_min_f32_e32 v246, v238, v246
	v_max_f32_e32 v238, v242, v250
	v_min_f32_e32 v250, v242, v250
	v_max_f32_e32 v242, v238, v246
	v_min_f32_e32 v246, v238, v246
	v_max_f32_e32 v238, v128, v244
	v_min_f32_e32 v244, v128, v244
	v_max_f32_e32 v128, v242, v243
	v_min_f32_e32 v243, v242, v243
	v_max_f32_e32 v242, v246, v252
	v_min_f32_e32 v252, v246, v252
	v_max_f32_e32 v246, v239, v247
	v_min_f32_e32 v247, v239, v247
	v_max_f32_e32 v239, v241, v249
	v_min_f32_e32 v249, v241, v249
	v_max_f32_e32 v241, v239, v247
	v_min_f32_e32 v247, v239, v247
	v_max_f32_e32 v239, v240, v248
	v_min_f32_e32 v248, v240, v248
	v_max_f32_e32 v240, v245, v253
	v_min_f32_e32 v253, v245, v253
	v_max_f32_e32 v245, v240, v248
	v_min_f32_e32 v248, v240, v248
	v_max_f32_e32 v240, v239, v241
	v_min_f32_e32 v241, v239, v241
	v_max_f32_e32 v239, v245, v247
	v_min_f32_e32 v247, v245, v247
	v_max_f32_e32 v245, v248, v249
	v_min_f32_e32 v249, v248, v249
	v_max_f32_e32 v248, v246, v238
	v_min_f32_e32 v238, v246, v238
	v_max_f32_e32 v246, v240, v244
	v_min_f32_e32 v244, v240, v244
	v_max_f32_e32 v240, v241, v128
	v_min_f32_e32 v128, v241, v128
	v_max_f32_e32 v241, v239, v243
	v_min_f32_e32 v243, v239, v243
	v_max_f32_e32 v239, v247, v242
	v_min_f32_e32 v242, v247, v242
	v_max_f32_e32 v247, v245, v252
	v_min_f32_e32 v252, v245, v252
	v_max_f32_e32 v245, v249, v250
	v_min_f32_e32 v250, v249, v250
	v_max_f32_e32 v236, v236, v253
	v_max_f32_e32 v254, v254, v250
	v_max_f32_e32 v226, v226, v245
	v_max_f32_e32 v225, v225, v252
	v_max_f32_e32 v229, v229, v247
	v_max_f32_e32 v232, v232, v242
	v_max_f32_e32 v234, v234, v239
	v_max_f32_e32 v233, v233, v243
	v_max_f32_e32 v230, v230, v241
	v_max_f32_e32 v231, v231, v128
	v_max_f32_e32 v235, v235, v240
	v_max_f32_e32 v228, v228, v244
	v_max_f32_e32 v222, v222, v246
; __device__ __forceinline__ float uniq_key(float s, int n) { return __uint_as_float((__float_as_uint(s) & ~0xffu) | (unsigned)(255 - n)); }
; #define INS16(A_, X_) do { float x_ = (X_); _Pragma("unroll") for (int i_ = 0; i_ < 16; ++i_) { const float hi_ = fmaxf(A_[i_], x_); x_ = fminf(A_[i_], x_); A_[i_] = hi_; } } while (0)
; __device__ __forceinline__ void p11_route(Frame& F) {
;     ...
;             for (int n = 0; n < PNK / 2; ++n) INS16(a, uniq_key(row[nb + n], nb + n));
;             float o[16];
; #pragma unroll
;             for (int i = 0; i < 16; ++i) o[i] = __builtin_bit_cast(float, __builtin_amdgcn_ds_bpermute(((F.lane + 32) & 63) << 2, __builtin_bit_cast(int, a[i])));
	v_max_f32_e32 v223, v223, v238
	v_max_f32_e32 v224, v224, v248
	v_max_f32_e32 v237, v237, v251
	v_max_f32_e32 v227, v236, v230
	v_min_f32_e32 v230, v236, v230
	v_max_f32_e32 v236, v254, v231
	v_min_f32_e32 v231, v254, v231
	v_max_f32_e32 v254, v226, v235
	v_min_f32_e32 v235, v226, v235
	v_max_f32_e32 v226, v225, v228
	v_min_f32_e32 v228, v225, v228
	v_max_f32_e32 v225, v229, v222
	v_min_f32_e32 v222, v229, v222
	v_max_f32_e32 v229, v232, v223
	v_min_f32_e32 v223, v232, v223
	v_max_f32_e32 v232, v234, v224
	v_min_f32_e32 v224, v234, v224
	v_max_f32_e32 v234, v233, v237
	v_min_f32_e32 v237, v233, v237
	v_max_f32_e32 v233, v227, v225
	v_min_f32_e32 v225, v227, v225
	v_max_f32_e32 v227, v236, v229
	v_min_f32_e32 v229, v236, v229
	v_max_f32_e32 v236, v254, v232
	v_min_f32_e32 v232, v254, v232
	v_max_f32_e32 v254, v226, v234
	v_min_f32_e32 v234, v226, v234
	v_max_f32_e32 v226, v230, v222
	v_min_f32_e32 v222, v230, v222
	v_max_f32_e32 v230, v231, v223
	v_min_f32_e32 v223, v231, v223
	v_max_f32_e32 v231, v235, v224
	v_min_f32_e32 v224, v235, v224
	v_max_f32_e32 v235, v228, v237
	v_min_f32_e32 v237, v228, v237
	v_max_f32_e32 v228, v233, v236
	v_min_f32_e32 v236, v233, v236
	v_max_f32_e32 v233, v227, v254
	v_min_f32_e32 v254, v227, v254
	v_max_f32_e32 v227, v225, v232
	v_min_f32_e32 v232, v225, v232
	v_max_f32_e32 v225, v229, v234
	v_min_f32_e32 v234, v229, v234
	v_max_f32_e32 v229, v226, v231
	v_min_f32_e32 v231, v226, v231
	v_max_f32_e32 v226, v230, v235
	v_min_f32_e32 v235, v230, v235
	v_max_f32_e32 v230, v222, v224
	v_min_f32_e32 v224, v222, v224
	v_max_f32_e32 v222, v223, v237
	v_min_f32_e32 v237, v223, v237
	v_max_f32_e32 v223, v228, v233
	v_min_f32_e32 v233, v228, v233
	v_max_f32_e32 v228, v236, v254
	v_min_f32_e32 v254, v236, v254
	v_max_f32_e32 v236, v227, v225
	v_min_f32_e32 v225, v227, v225
	v_max_f32_e32 v227, v232, v234
	v_min_f32_e32 v234, v232, v234
	v_max_f32_e32 v232, v229, v226
	v_min_f32_e32 v226, v229, v226
	v_max_f32_e32 v229, v231, v235
	v_min_f32_e32 v235, v231, v235
	v_max_f32_e32 v231, v230, v222
	v_min_f32_e32 v222, v230, v222
	v_max_f32_e32 v230, v224, v237
	v_min_f32_e32 v237, v224, v237
	v_mov_b32_e32 v137, v223
	v_mov_b32_e32 v139, v233
	v_mov_b32_e32 v140, v228
	v_mov_b32_e32 v141, v254
	v_mov_b32_e32 v142, v236
	v_mov_b32_e32 v143, v225
	v_mov_b32_e32 v144, v227
	v_mov_b32_e32 v145, v234
	v_mov_b32_e32 v147, v232
	v_mov_b32_e32 v148, v226
	v_mov_b32_e32 v149, v229
	v_mov_b32_e32 v159, v235
	v_mov_b32_e32 v161, v231
	v_mov_b32_e32 v162, v222
	v_mov_b32_e32 v160, v230
	v_mov_b32_e32 v129, v237
	ds_bpermute_b32 v166, v153, v137
	ds_bpermute_b32 v165, v153, v139
	ds_bpermute_b32 v164, v153, v140
	ds_bpermute_b32 v163, v153, v141
	ds_bpermute_b32 v146, v153, v142
	ds_bpermute_b32 v138, v153, v143
	ds_bpermute_b32 v136, v153, v144
	ds_bpermute_b32 v135, v153, v145
	ds_bpermute_b32 v134, v153, v147
	ds_bpermute_b32 v133, v153, v148
	ds_bpermute_b32 v132, v153, v149
	ds_bpermute_b32 v131, v153, v159
	ds_bpermute_b32 v130, v153, v161
	ds_bpermute_b32 v128, v153, v162
	ds_bpermute_b32 v127, v153, v160
	ds_bpermute_b32 v126, v153, v129
	s_and_saveexec_b64 s[4:5], s[0:1]
	s_cbranch_execz .LBB0_3218
; #define INS16(A_, X_) do { float x_ = (X_); _Pragma("unroll") for (int i_ = 0; i_ < 16; ++i_) { const float hi_ = fmaxf(A_[i_], x_); x_ = fminf(A_[i_], x_); A_[i_] = hi_; } } while (0)
; __device__ __forceinline__ void p11_route(Frame& F) {
;     ...
;             for (int i = 0; i < 16; ++i) o[i] = __builtin_bit_cast(float, __builtin_amdgcn_ds_bpermute(((F.lane + 32) & 63) << 2, __builtin_bit_cast(int, a[i])));
; #pragma unroll
;             for (int i = 0; i < 16; ++i) INS16(a, o[i]);
;           if (F.lane < 32) {
;             float tv[16]; int ti[16];
; #pragma unroll
;             for (int i = 0; i < 16; ++i) { ti[i] = 255 - (int)(__float_as_uint(a[i]) & 255u); tv[i] = row[ti[i]]; }
; #pragma unroll
;             for (int i = 0; i < 16; ++i) { row[i] = tv[i]; row[16 + i] = __int_as_float(ti[i]); }
;           } }
	s_waitcnt lgkmcnt(0)
	v_max_f32_e32 v222, v137, v126
	v_max_f32_e32 v223, v139, v127
	v_max_f32_e32 v224, v140, v128
	v_max_f32_e32 v225, v141, v130
	v_max_f32_e32 v226, v142, v131
	v_max_f32_e32 v227, v143, v132
	v_max_f32_e32 v228, v144, v133
	v_max_f32_e32 v229, v145, v134
	v_max_f32_e32 v230, v147, v135
	v_max_f32_e32 v231, v148, v136
	v_max_f32_e32 v232, v149, v138
	v_max_f32_e32 v233, v159, v146
	v_max_f32_e32 v234, v161, v163
	v_max_f32_e32 v235, v162, v164
	v_max_f32_e32 v236, v160, v165
	v_max_f32_e32 v237, v129, v166
	v_max_f32_e32 v254, v222, v230
	v_min_f32_e32 v230, v222, v230
	v_max_f32_e32 v222, v223, v231
	v_min_f32_e32 v231, v223, v231
	v_max_f32_e32 v223, v224, v232
	v_min_f32_e32 v232, v224, v232
	v_max_f32_e32 v224, v225, v233
	v_min_f32_e32 v233, v225, v233
	v_max_f32_e32 v225, v226, v234
	v_min_f32_e32 v234, v226, v234
	v_max_f32_e32 v226, v227, v235
	v_min_f32_e32 v235, v227, v235
	v_max_f32_e32 v227, v228, v236
	v_min_f32_e32 v236, v228, v236
	v_max_f32_e32 v228, v229, v237
	v_min_f32_e32 v237, v229, v237
	v_max_f32_e32 v229, v254, v225
	v_min_f32_e32 v225, v254, v225
	v_max_f32_e32 v254, v222, v226
	v_min_f32_e32 v226, v222, v226
	v_max_f32_e32 v222, v223, v227
	v_min_f32_e32 v227, v223, v227
	v_max_f32_e32 v223, v224, v228
	v_min_f32_e32 v228, v224, v228
	v_max_f32_e32 v224, v230, v234
	v_min_f32_e32 v234, v230, v234
	v_max_f32_e32 v230, v231, v235
	v_min_f32_e32 v235, v231, v235
	v_max_f32_e32 v231, v232, v236
	v_min_f32_e32 v236, v232, v236
	v_max_f32_e32 v232, v233, v237
	v_min_f32_e32 v237, v233, v237
	v_max_f32_e32 v233, v229, v222
	v_min_f32_e32 v222, v229, v222
	v_max_f32_e32 v229, v254, v223
	v_min_f32_e32 v223, v254, v223
	v_max_f32_e32 v254, v225, v227
	v_min_f32_e32 v227, v225, v227
	v_max_f32_e32 v225, v226, v228
	v_min_f32_e32 v228, v226, v228
	v_max_f32_e32 v226, v224, v231
	v_min_f32_e32 v231, v224, v231
	v_max_f32_e32 v224, v230, v232
	v_min_f32_e32 v232, v230, v232
	v_max_f32_e32 v230, v234, v236
	v_min_f32_e32 v236, v234, v236
	v_max_f32_e32 v234, v235, v237
	v_min_f32_e32 v237, v235, v237
	v_max_f32_e32 v235, v233, v229
	v_min_f32_e32 v229, v233, v229
	v_max_f32_e32 v233, v222, v223
	v_min_f32_e32 v223, v222, v223
	v_max_f32_e32 v222, v254, v225
	v_min_f32_e32 v225, v254, v225
	v_max_f32_e32 v254, v227, v228
	v_min_f32_e32 v228, v227, v228
	v_max_f32_e32 v227, v226, v224
	v_min_f32_e32 v224, v226, v224
	v_max_f32_e32 v226, v231, v232
	v_min_f32_e32 v232, v231, v232
	v_max_f32_e32 v231, v230, v234
	v_min_f32_e32 v234, v230, v234
	v_max_f32_e32 v230, v236, v237
	v_min_f32_e32 v237, v236, v237
	v_mov_b32_e32 v126, v235
	v_mov_b32_e32 v127, v229
	v_mov_b32_e32 v128, v233
	v_mov_b32_e32 v130, v223
	v_mov_b32_e32 v131, v222
	v_mov_b32_e32 v132, v225
	v_mov_b32_e32 v133, v254
	v_mov_b32_e32 v134, v228
	v_mov_b32_e32 v135, v227
	v_mov_b32_e32 v136, v224
	v_mov_b32_e32 v137, v226
	v_mov_b32_e32 v138, v232
	v_mov_b32_e32 v139, v231
	v_mov_b32_e32 v140, v234
	v_mov_b32_e32 v141, v230
	v_mov_b32_e32 v129, v237
	v_xor_b32_e32 v127, -1, v127
	v_xor_b32_e32 v126, -1, v126
	v_xor_b32_e32 v130, -1, v130
	v_xor_b32_e32 v128, -1, v128
	v_xor_b32_e32 v132, -1, v132
	v_xor_b32_e32 v131, -1, v131
	v_xor_b32_e32 v134, -1, v134
	v_xor_b32_e32 v133, -1, v133
	v_xor_b32_e32 v136, -1, v136
	v_xor_b32_e32 v135, -1, v135
	v_xor_b32_e32 v138, -1, v138
	v_xor_b32_e32 v137, -1, v137
	v_xor_b32_e32 v140, -1, v140
	v_xor_b32_e32 v139, -1, v139
	v_xor_b32_e32 v129, -1, v129
	v_xor_b32_e32 v141, -1, v141
	v_and_b32_e32 v127, 0xff, v127
	v_and_b32_e32 v126, 0xff, v126
	v_and_b32_e32 v130, 0xff, v130
	v_and_b32_e32 v128, 0xff, v128
	v_and_b32_e32 v132, 0xff, v132
	v_and_b32_e32 v131, 0xff, v131
	v_and_b32_e32 v134, 0xff, v134
	v_and_b32_e32 v133, 0xff, v133
	v_and_b32_e32 v136, 0xff, v136
	v_and_b32_e32 v135, 0xff, v135
	v_and_b32_e32 v138, 0xff, v138
	v_and_b32_e32 v137, 0xff, v137
	v_and_b32_e32 v140, 0xff, v140
	v_and_b32_e32 v139, 0xff, v139
	v_and_b32_e32 v129, 0xff, v129
	v_and_b32_e32 v141, 0xff, v141
	v_lshl_add_u32 v142, v126, 2, v152
	v_lshl_add_u32 v143, v127, 2, v152
	v_lshl_add_u32 v144, v128, 2, v152
	v_lshl_add_u32 v145, v130, 2, v152
	v_lshl_add_u32 v146, v131, 2, v152
	v_lshl_add_u32 v147, v132, 2, v152
	v_lshl_add_u32 v148, v133, 2, v152
	v_lshl_add_u32 v149, v134, 2, v152
	v_lshl_add_u32 v159, v135, 2, v152
	v_lshl_add_u32 v160, v136, 2, v152
	v_lshl_add_u32 v161, v137, 2, v152
	v_lshl_add_u32 v162, v138, 2, v152
	v_lshl_add_u32 v163, v139, 2, v152
	v_lshl_add_u32 v164, v140, 2, v152
	v_lshl_add_u32 v165, v141, 2, v152
	v_lshl_add_u32 v166, v129, 2, v152
	ds_read_b32 v142, v142
	ds_read_b32 v143, v143
	ds_read_b32 v144, v144
	ds_read_b32 v145, v145
	ds_read_b32 v146, v146
	ds_read_b32 v147, v147
	ds_read_b32 v148, v148
	ds_read_b32 v149, v149
	ds_read_b32 v159, v159
	ds_read_b32 v160, v160
	ds_read_b32 v161, v161
	ds_read_b32 v162, v162
	ds_read_b32 v163, v163
	ds_read_b32 v164, v164
	ds_read_b32 v165, v165
	ds_read_b32 v166, v166
	s_waitcnt lgkmcnt(14)
	ds_write2_b32 v152, v142, v143 offset1:1
	ds_write2_b32 v152, v126, v127 offset0:16 offset1:17
	s_waitcnt lgkmcnt(14)
	ds_write2_b32 v152, v144, v145 offset0:2 offset1:3
	ds_write2_b32 v152, v128, v130 offset0:18 offset1:19
	s_waitcnt lgkmcnt(14)
	ds_write2_b32 v152, v146, v147 offset0:4 offset1:5
	ds_write2_b32 v152, v131, v132 offset0:20 offset1:21
	s_waitcnt lgkmcnt(14)
	ds_write2_b32 v152, v148, v149 offset0:6 offset1:7
	ds_write2_b32 v152, v133, v134 offset0:22 offset1:23
	s_waitcnt lgkmcnt(14)
	ds_write2_b32 v152, v159, v160 offset0:8 offset1:9
	ds_write2_b32 v152, v135, v136 offset0:24 offset1:25
	s_waitcnt lgkmcnt(14)
	ds_write2_b32 v152, v161, v162 offset0:10 offset1:11
	ds_write2_b32 v152, v137, v138 offset0:26 offset1:27
	s_waitcnt lgkmcnt(14)
	ds_write2_b32 v152, v163, v164 offset0:12 offset1:13
	ds_write2_b32 v152, v139, v140 offset0:28 offset1:29
	s_waitcnt lgkmcnt(14)
	ds_write2_b32 v152, v165, v166 offset0:14 offset1:15
	ds_write2_b32 v152, v141, v129 offset0:30 offset1:31
	s_or_b64 exec, exec, s[4:5]
	s_and_saveexec_b64 s[12:13], s[2:3]
	s_cbranch_execz .LBB0_3213
	s_branch .LBB0_3219
